# speedup vs baseline: 1.0818x; 1.0036x over previous
_Z22k2_resolve_rank_gatherPKfS0_PKdS0_PKiPKyPKtS0_S4_Pf:
	s_load_dwordx16 s[4:19], s[0:1], 0x0
	s_load_dwordx4 s[20:23], s[0:1], 0x40
	s_and_b32 s3, s2, 7
	s_lshr_b32 s2, s2, 3
	s_lshl_b32 s3, s3, 7
	s_add_u32 s2, s2, s3
	v_and_b32_e32 v1, 0x3ff, v0
	s_lshr_b32 s24, s2, 6
	s_and_b32 s25, s2, 63
	s_lshl_b32 s26, s24, 9
	v_lshl_add_u32 v2, v1, 1, s26
	v_lshlrev_b32_e32 v3, 4, v2
	v_lshlrev_b32_e32 v24, 2, v2
	v_lshlrev_b32_e32 v25, 3, v2
	v_mov_b32_e32 v106, 0
	v_mov_b32_e32 v107, 0
	v_mov_b32_e32 v105, 0x1800
	v_lshlrev_b32_e32 v104, 3, v1
	s_movk_i32 s30, 0x641
	s_mov_b32 s32, 0xa0b5ed8d
	s_mov_b32 s33, 0x3ed0c6f7
	s_mov_b32 s34, 0xa0b5ed8d
	s_mov_b32 s35, 0xbed0c6f7
	s_mul_i32 s31, s26, 0x1904
	v_lshrrev_b32_e32 v29, 6, v1
	s_waitcnt lgkmcnt(0)
	global_load_dwordx4 v[4:7], v3, s[16:17]
	global_load_dwordx4 v[8:11], v3, s[16:17] offset:16
	global_load_dwordx2 v[12:13], v24, s[10:11]
	global_load_dwordx2 v[16:17], v24, s[12:13]
	global_load_dwordx4 v[20:23], v25, s[8:9]
	global_load_dwordx2 v[14:15], v24, s[18:19]
	global_load_dwordx2 v[18:19], v24, s[20:21]
	s_add_u32 s28, s4, s31
	s_addc_u32 s29, s5, 0
	v_readfirstlane_b32 s27, v29
	ds_write_b64 v105, v[106:107]
	ds_write_b64 v105, v[106:107] offset:8
	ds_write_b64 v105, v[106:107] offset:16
	ds_write_b64 v105, v[106:107] offset:24
	ds_write_b64 v104, v[106:107] offset:8448
	s_mov_b64 s[36:37], 0
	s_mov_b64 s[38:39], 0
	s_mov_b64 s[40:41], 0
	s_mov_b64 s[42:43], 0
	s_mov_b64 s[44:45], 0
	v_lshlrev_b32_e32 v2, 4, v1
	s_waitcnt vmcnt(2)
	ds_write_b128 v2, v[20:23] offset:12544
	v_lshlrev_b32_e32 v3, 5, v1
	ds_write_b128 v3, v[4:7] offset:22784
	ds_write_b128 v3, v[8:11] offset:22800
	ds_write_b64 v104, v[16:17] offset:30976
	v_and_b32_e32 v26, 0xffff, v4
	v_and_b32_e32 v27, 0xffff, v8
	v_max_u32_e32 v28, v26, v27
	v_cvt_f64_f32_e32 v[92:93], v12
	v_cvt_f64_f32_e32 v[94:95], v13
	v_add_f64 v[92:93], v[92:93], -v[20:21]
	v_add_f64 v[94:95], v[94:95], -v[22:23]
	ds_write_b128 v2, v[92:95] offset:0
	ds_write_b64 v104, v[12:13] offset:4096
	s_waitcnt vmcnt(0)
	ds_write_b64 v104, v[14:15] offset:33024
	v_cvt_f64_f32_e32 v[96:97], v14
	v_cvt_f64_f32_e32 v[98:99], v15
	v_add_f64 v[96:97], v[96:97], -v[20:21]
	v_add_f64 v[98:99], v[98:99], -v[22:23]
	v_cmp_lt_u32_e32 vcc, 0, v28
	s_cbranch_vccz .Lk2_l1a_done
	v_cmp_lt_u32_e32 vcc, 0, v26
	s_and_saveexec_b64 s[46:47], vcc
	s_cbranch_execz .Lk2_l1a_0_0
	v_lshrrev_b32_e32 v29, 16, v4
	v_mad_u32_u24 v30, v29, s30, v16
	v_lshlrev_b32_e32 v30, 2, v30
	global_load_dword v32, v30, s[28:29]
.Lk2_l1a_0_0:
	s_or_b64 exec, exec, s[46:47]
	v_cmp_lt_u32_e32 vcc, 0, v27
	s_and_saveexec_b64 s[46:47], vcc
	s_cbranch_execz .Lk2_l1a_0_1
	v_lshrrev_b32_e32 v29, 16, v8
	v_mad_u32_u24 v30, v29, s30, v17
	v_lshlrev_b32_e32 v30, 2, v30
	global_load_dword v36, v30, s[28:29]
.Lk2_l1a_0_1:
	s_or_b64 exec, exec, s[46:47]
	v_cmp_lt_u32_e32 vcc, 1, v28
	s_cbranch_vccz .Lk2_l1a_done
	v_cmp_lt_u32_e32 vcc, 1, v26
	s_and_saveexec_b64 s[46:47], vcc
	s_cbranch_execz .Lk2_l1a_1_0
	v_and_b32_e32 v29, 0xffff, v5
	v_mad_u32_u24 v30, v29, s30, v16
	v_lshlrev_b32_e32 v30, 2, v30
	global_load_dword v40, v30, s[28:29]
.Lk2_l1a_1_0:
	s_or_b64 exec, exec, s[46:47]
	v_cmp_lt_u32_e32 vcc, 1, v27
	s_and_saveexec_b64 s[46:47], vcc
	s_cbranch_execz .Lk2_l1a_1_1
	v_and_b32_e32 v29, 0xffff, v9
	v_mad_u32_u24 v30, v29, s30, v17
	v_lshlrev_b32_e32 v30, 2, v30
	global_load_dword v44, v30, s[28:29]
.Lk2_l1a_1_1:
	s_or_b64 exec, exec, s[46:47]
	v_cmp_lt_u32_e32 vcc, 2, v28
	s_cbranch_vccz .Lk2_l1a_done
	v_cmp_lt_u32_e32 vcc, 2, v26
	s_and_saveexec_b64 s[46:47], vcc
	s_cbranch_execz .Lk2_l1a_2_0
	v_lshrrev_b32_e32 v29, 16, v5
	v_mad_u32_u24 v30, v29, s30, v16
	v_lshlrev_b32_e32 v30, 2, v30
	global_load_dword v48, v30, s[28:29]
.Lk2_l1a_2_0:
	s_or_b64 exec, exec, s[46:47]
	v_cmp_lt_u32_e32 vcc, 2, v27
	s_and_saveexec_b64 s[46:47], vcc
	s_cbranch_execz .Lk2_l1a_2_1
	v_lshrrev_b32_e32 v29, 16, v9
	v_mad_u32_u24 v30, v29, s30, v17
	v_lshlrev_b32_e32 v30, 2, v30
	global_load_dword v52, v30, s[28:29]
.Lk2_l1a_2_1:
	s_or_b64 exec, exec, s[46:47]
	v_cmp_lt_u32_e32 vcc, 3, v28
	s_cbranch_vccz .Lk2_l1a_done
	v_cmp_lt_u32_e32 vcc, 3, v26
	s_and_saveexec_b64 s[46:47], vcc
	s_cbranch_execz .Lk2_l1a_3_0
	v_and_b32_e32 v29, 0xffff, v6
	v_mad_u32_u24 v30, v29, s30, v16
	v_lshlrev_b32_e32 v30, 2, v30
	global_load_dword v56, v30, s[28:29]
.Lk2_l1a_3_0:
	s_or_b64 exec, exec, s[46:47]
	v_cmp_lt_u32_e32 vcc, 3, v27
	s_and_saveexec_b64 s[46:47], vcc
	s_cbranch_execz .Lk2_l1a_3_1
	v_and_b32_e32 v29, 0xffff, v10
	v_mad_u32_u24 v30, v29, s30, v17
	v_lshlrev_b32_e32 v30, 2, v30
	global_load_dword v60, v30, s[28:29]
.Lk2_l1a_3_1:
	s_or_b64 exec, exec, s[46:47]
	v_cmp_lt_u32_e32 vcc, 4, v28
	s_cbranch_vccz .Lk2_l1a_done
	v_cmp_lt_u32_e32 vcc, 4, v26
	s_and_saveexec_b64 s[46:47], vcc
	s_cbranch_execz .Lk2_l1a_4_0
	v_lshrrev_b32_e32 v29, 16, v6
	v_mad_u32_u24 v30, v29, s30, v16
	v_lshlrev_b32_e32 v30, 2, v30
	global_load_dword v64, v30, s[28:29]
.Lk2_l1a_4_0:
	s_or_b64 exec, exec, s[46:47]
	v_cmp_lt_u32_e32 vcc, 4, v27
	s_and_saveexec_b64 s[46:47], vcc
	s_cbranch_execz .Lk2_l1a_4_1
	v_lshrrev_b32_e32 v29, 16, v10
	v_mad_u32_u24 v30, v29, s30, v17
	v_lshlrev_b32_e32 v30, 2, v30
	global_load_dword v68, v30, s[28:29]
.Lk2_l1a_4_1:
	s_or_b64 exec, exec, s[46:47]
	v_cmp_lt_u32_e32 vcc, 5, v28
	s_cbranch_vccz .Lk2_l1a_done
	v_cmp_lt_u32_e32 vcc, 5, v26
	s_and_saveexec_b64 s[46:47], vcc
	s_cbranch_execz .Lk2_l1a_5_0
	v_and_b32_e32 v29, 0xffff, v7
	v_mad_u32_u24 v30, v29, s30, v16
	v_lshlrev_b32_e32 v30, 2, v30
	global_load_dword v72, v30, s[28:29]
.Lk2_l1a_5_0:
	s_or_b64 exec, exec, s[46:47]
	v_cmp_lt_u32_e32 vcc, 5, v27
	s_and_saveexec_b64 s[46:47], vcc
	s_cbranch_execz .Lk2_l1a_5_1
	v_and_b32_e32 v29, 0xffff, v11
	v_mad_u32_u24 v30, v29, s30, v17
	v_lshlrev_b32_e32 v30, 2, v30
	global_load_dword v76, v30, s[28:29]
.Lk2_l1a_5_1:
	s_or_b64 exec, exec, s[46:47]
	v_cmp_lt_u32_e32 vcc, 6, v28
	s_cbranch_vccz .Lk2_l1a_done
	v_cmp_lt_u32_e32 vcc, 6, v26
	s_and_saveexec_b64 s[46:47], vcc
	s_cbranch_execz .Lk2_l1a_6_0
	v_lshrrev_b32_e32 v29, 16, v7
	v_mad_u32_u24 v30, v29, s30, v16
	v_lshlrev_b32_e32 v30, 2, v30
	global_load_dword v80, v30, s[28:29]
.Lk2_l1a_6_0:
	s_or_b64 exec, exec, s[46:47]
	v_cmp_lt_u32_e32 vcc, 6, v27
	s_and_saveexec_b64 s[46:47], vcc
	s_cbranch_execz .Lk2_l1a_6_1
	v_lshrrev_b32_e32 v29, 16, v11
	v_mad_u32_u24 v30, v29, s30, v17
	v_lshlrev_b32_e32 v30, 2, v30
	global_load_dword v84, v30, s[28:29]
